# v21: v16 + NSA rescale-test ballot trimmed to wave-mask SALU logic (3 sites) + canonicalising self-max folded out of the row-max (12 sites)
# speedup vs baseline: 1.0028x; 1.0028x over previous
.LBB0_734:
	s_nop 9
	v_max_f32_e32 v39, v4, v8
	v_max_f32_e32 v41, v5, v9
	v_max_f32_e32 v42, v7, v11
	v_max3_f32 v43, v6, v10, v14
	v_max3_f32 v42, v42, v15, v19
	v_max3_f32 v39, v39, v12, v16
	v_max3_f32 v41, v41, v13, v17
	v_max3_f32 v43, v43, v18, v22
	v_max3_f32 v42, v42, v23, v27
	v_max3_f32 v39, v39, v20, v24
	v_max3_f32 v41, v41, v21, v25
	v_max3_f32 v43, v43, v26, v30
	v_max3_f32 v42, v42, v31, v35
	v_max3_f32 v39, v39, v28, v32
	v_max3_f32 v41, v41, v29, v33
	v_max3_f32 v42, v43, v34, v42
	v_max3_f32 v39, v39, v41, v42
	v_mov_b32_e32 v41, v39
	s_nop 1
	v_permlane32_swap_b32_e32 v39, v41
	v_max_f32_e32 v41, v39, v41
	v_cmp_lt_f32_e64 s[10:11], s16, v41
	v_cmp_neq_f32_e32 vcc, s4, v41
	v_mov_b32_e32 v39, 1.0
	s_andn2_b64 s[12:13], vcc, s[8:9]
	s_and_b64 vcc, s[10:11], s[8:9]
	s_or_b64 s[12:13], s[12:13], vcc
	s_cbranch_scc1 .LBB0_737

.LBB0_797:
	s_nop 8
	v_max_f32_e32 v2, v68, v72
	v_max_f32_e32 v193, v69, v73
	v_max_f32_e32 v194, v71, v75
	v_max3_f32 v195, v70, v74, v78
	v_max3_f32 v194, v194, v79, v83
	v_max3_f32 v2, v2, v76, v80
	v_max3_f32 v193, v193, v77, v81
	v_max3_f32 v195, v195, v82, v86
	v_max3_f32 v194, v194, v87, v91
	v_max3_f32 v2, v2, v84, v88
	v_max3_f32 v193, v193, v85, v89
	v_max3_f32 v195, v195, v90, v94
	v_max3_f32 v194, v194, v95, v99
	v_max3_f32 v2, v2, v92, v96
	v_max3_f32 v193, v193, v93, v97
	v_max3_f32 v194, v195, v98, v194
	v_max3_f32 v2, v2, v193, v194
	v_mov_b32_e32 v193, v2
	s_nop 1
	v_permlane32_swap_b32_e32 v2, v193
	v_max_f32_e32 v2, v2, v193
	v_cmp_lt_f32_e64 s[12:13], s16, v2
	v_cmp_neq_f32_e32 vcc, s4, v2
	v_mov_b32_e32 v193, 1.0
	s_andn2_b64 s[14:15], vcc, s[10:11]
	s_and_b64 vcc, s[12:13], s[10:11]
	s_or_b64 s[14:15], s[14:15], vcc
	s_cbranch_scc1 .LBB0_804
	v_cmp_gt_f32_e32 vcc, 1.0, v193
	s_cbranch_vccz .LBB0_802

.LBB0_978:
	s_nop 9
	v_max_f32_e32 v2, v68, v72
	v_max_f32_e32 v214, v69, v73
	v_max_f32_e32 v215, v71, v75
	v_max3_f32 v216, v70, v74, v78
	v_max3_f32 v215, v215, v79, v83
	v_max3_f32 v2, v2, v76, v80
	v_max3_f32 v214, v214, v77, v81
	v_max3_f32 v216, v216, v82, v86
	v_max3_f32 v215, v215, v87, v91
	v_max3_f32 v2, v2, v84, v88
	v_max3_f32 v214, v214, v85, v89
	v_max3_f32 v216, v216, v90, v94
	v_max3_f32 v215, v215, v95, v99
	v_max3_f32 v2, v2, v92, v96
	v_max3_f32 v214, v214, v93, v97
	v_max3_f32 v215, v216, v98, v215
	v_max3_f32 v2, v2, v214, v215
	v_mov_b32_e32 v214, v2
	s_nop 1
	v_permlane32_swap_b32_e32 v2, v214
	v_max_f32_e32 v2, v2, v214
	v_cmp_lt_f32_e64 s[12:13], s16, v2
	v_cmp_neq_f32_e32 vcc, s4, v2
	v_mov_b32_e32 v214, 1.0
	s_andn2_b64 s[14:15], vcc, s[10:11]
	s_and_b64 vcc, s[12:13], s[10:11]
	s_or_b64 s[14:15], s[14:15], vcc
	s_cbranch_scc1 .LBB0_985
	v_cmp_gt_f32_e32 vcc, 1.0, v214
	s_cbranch_vccz .LBB0_983
